# stream: wave-row rotation by blk + (blk>>3) so CUs of one XCD also spread over stacks
# speedup vs baseline: 1.0032x; 1.0032x over previous
.LBB1_2:
	s_or_b64 exec, exec, s[0:1]
	s_lshr_b32 s8, s3, 6
	s_lshr_b32 s9, s2, 3
	s_add_i32 s8, s8, s9
	s_add_i32 s8, s8, s2
	s_and_b32 s8, s8, 15
	s_lshl_b32 s0, s2, 7
	v_and_b32_e32 v24, 63, v0
	s_add_i32 s9, s8, s0
	s_waitcnt lgkmcnt(0)
	s_and_b32 s1, s5, 0xffff
	s_mov_b32 s3, 0x20000
	s_brev_b32 s2, 16
	s_mov_b32 s0, s4
	v_lshlrev_b32_e32 v25, 4, v24
	s_lshl_b32 s4, s9, 12
	buffer_load_dwordx4 v[26:29], v25, s[0:3], s4 offen offset:1024 nt
	buffer_load_dwordx4 v[30:33], v25, s[0:3], s4 offen nt
	buffer_load_dwordx4 v[34:37], v25, s[0:3], s4 offen offset:2048 nt
	s_add_i32 s5, s4, 0x10000
	buffer_load_dwordx4 v[38:41], v25, s[0:3], s5 offen offset:1024 nt
	buffer_load_dwordx4 v[42:45], v25, s[0:3], s5 offen nt
	buffer_load_dwordx4 v[16:19], v25, s[0:3], s4 offen offset:3072 nt
	s_add_i32 s10, s4, 0x20000
	buffer_load_dwordx4 v[46:49], v25, s[0:3], s5 offen offset:2048 nt
	buffer_load_dwordx4 v[20:23], v25, s[0:3], s5 offen offset:3072 nt
	s_barrier
	buffer_load_dwordx4 v[50:53], v25, s[0:3], s10 offen offset:1024 nt
	buffer_load_dwordx4 v[54:57], v25, s[0:3], s10 offen nt
	ds_read_b128 v[4:7], v25 offset:1024
	ds_read_b128 v[0:3], v25
	ds_read_b128 v[12:15], v25 offset:2048
	ds_read_b128 v[8:11], v25 offset:3072
	s_add_i32 s5, s4, 0x30000
	v_cmp_gt_u32_e32 vcc, 8, v24
	s_waitcnt vmcnt(9) lgkmcnt(3)
	v_pk_mul_f32 v[28:29], v[6:7], v[28:29]
	v_pk_mul_f32 v[26:27], v[4:5], v[26:27]
	s_waitcnt vmcnt(8) lgkmcnt(2)
	v_pk_fma_f32 v[32:33], v[2:3], v[32:33], v[28:29]
	v_pk_fma_f32 v[30:31], v[0:1], v[30:31], v[26:27]
	buffer_load_dwordx4 v[26:29], v25, s[0:3], s5 offen offset:1024 nt
	s_waitcnt vmcnt(8) lgkmcnt(1)
	v_pk_fma_f32 v[58:59], v[14:15], v[36:37], v[32:33]
	v_pk_fma_f32 v[60:61], v[12:13], v[34:35], v[30:31]
	buffer_load_dwordx4 v[30:33], v25, s[0:3], s5 offen nt
	s_waitcnt vmcnt(8)
	v_pk_mul_f32 v[34:35], v[6:7], v[40:41]
	v_pk_mul_f32 v[36:37], v[4:5], v[38:39]
	s_waitcnt vmcnt(7)
	v_pk_fma_f32 v[44:45], v[2:3], v[44:45], v[34:35]
	v_pk_fma_f32 v[42:43], v[0:1], v[42:43], v[36:37]
	buffer_load_dwordx4 v[34:37], v25, s[0:3], s10 offen offset:2048 nt
	s_waitcnt vmcnt(4)
	v_pk_mul_f32 v[38:39], v[6:7], v[52:53]
	v_pk_mul_f32 v[40:41], v[4:5], v[50:51]
	s_waitcnt vmcnt(3)
	v_pk_fma_f32 v[50:51], v[2:3], v[56:57], v[38:39]
	v_pk_fma_f32 v[52:53], v[0:1], v[54:55], v[40:41]
	buffer_load_dwordx4 v[38:41], v25, s[0:3], s10 offen offset:3072 nt
	v_pk_fma_f32 v[48:49], v[14:15], v[48:49], v[44:45]
	v_pk_fma_f32 v[46:47], v[12:13], v[46:47], v[42:43]
	s_waitcnt lgkmcnt(0)
	v_pk_fma_f32 v[18:19], v[10:11], v[18:19], v[58:59]
	v_pk_fma_f32 v[16:17], v[8:9], v[16:17], v[60:61]
	v_add_f32_e32 v61, v18, v19
	v_add_f32_e32 v60, v16, v17
	v_pk_fma_f32 v[16:17], v[10:11], v[22:23], v[48:49]
	v_pk_fma_f32 v[18:19], v[8:9], v[20:21], v[46:47]
	v_add_f32_e32 v16, v16, v17
	v_add_f32_e32 v18, v18, v19
	v_add_f32_e32 v60, v60, v61
	v_add_f32_e32 v16, v18, v16
	s_add_i32 s10, s4, 0x50000
	s_waitcnt vmcnt(3)
	v_pk_mul_f32 v[28:29], v[6:7], v[28:29]
	v_pk_mul_f32 v[26:27], v[4:5], v[26:27]
	v_add_f32_dpp v16, v16, v16 quad_perm:[1,0,3,2] row_mask:0xf bank_mask:0xf bound_ctrl:1
	s_waitcnt vmcnt(2)
	v_pk_fma_f32 v[54:55], v[2:3], v[32:33], v[28:29]
	v_pk_fma_f32 v[56:57], v[0:1], v[30:31], v[26:27]
	buffer_load_dwordx4 v[26:29], v25, s[0:3], s5 offen offset:2048 nt
	buffer_load_dwordx4 v[30:33], v25, s[0:3], s5 offen offset:3072 nt
	s_add_i32 s5, s4, 0x40000
	buffer_load_dwordx4 v[42:45], v25, s[0:3], s5 offen offset:1024 nt
	s_waitcnt vmcnt(4)
	v_pk_fma_f32 v[50:51], v[14:15], v[36:37], v[50:51]
	v_pk_fma_f32 v[52:53], v[12:13], v[34:35], v[52:53]
	buffer_load_dwordx4 v[34:37], v25, s[0:3], s5 offen nt
	v_add_f32_dpp v16, v16, v16 quad_perm:[2,3,0,1] row_mask:0xf bank_mask:0xf bound_ctrl:1
	s_waitcnt vmcnt(4)
	v_pk_fma_f32 v[58:59], v[10:11], v[40:41], v[50:51]
	v_pk_fma_f32 v[38:39], v[8:9], v[38:39], v[52:53]
	v_add_f32_e32 v19, v58, v59
	v_add_f32_e32 v17, v38, v39
	v_add_f32_dpp v58, v60, v60 quad_perm:[1,0,3,2] row_mask:0xf bank_mask:0xf bound_ctrl:1
	v_add_f32_e32 v18, v17, v19
	v_add_f32_dpp v16, v16, v16 row_ror:4 row_mask:0xf bank_mask:0xf bound_ctrl:1
	v_add_f32_dpp v17, v58, v58 quad_perm:[2,3,0,1] row_mask:0xf bank_mask:0xf bound_ctrl:1
	buffer_load_dwordx4 v[20:23], v25, s[0:3], s5 offen offset:2048 nt
	buffer_load_dwordx4 v[46:49], v25, s[0:3], s5 offen offset:3072 nt
	v_add_f32_dpp v17, v17, v17 row_ror:4 row_mask:0xf bank_mask:0xf bound_ctrl:1
	v_add_f32_dpp v58, v16, v16 row_ror:8 row_mask:0xf bank_mask:0xf bound_ctrl:1
	buffer_load_dwordx4 v[38:41], v25, s[0:3], s10 offen nt
	buffer_load_dwordx4 v[50:53], v25, s[0:3], s10 offen offset:1024 nt
	v_add_f32_dpp v17, v17, v17 row_ror:8 row_mask:0xf bank_mask:0xf bound_ctrl:1
	v_mov_b32_e32 v19, v17
	v_mov_b32_e32 v59, v58
	s_nop 0
	v_permlane16_swap_b32_e32 v17, v19
	v_permlane16_swap_b32_e32 v58, v59
	v_add_f32_e32 v16, v17, v19
	v_add_f32_e32 v17, v58, v59
	s_add_i32 s5, s4, 0x60000
	s_add_i32 s4, s4, 0x70000
	v_add_f32_dpp v18, v18, v18 quad_perm:[1,0,3,2] row_mask:0xf bank_mask:0xf bound_ctrl:1
	s_waitcnt vmcnt(7)
	v_pk_fma_f32 v[28:29], v[14:15], v[28:29], v[54:55]
	v_pk_fma_f32 v[54:55], v[12:13], v[26:27], v[56:57]
	s_waitcnt vmcnt(6)
	v_pk_fma_f32 v[58:59], v[10:11], v[32:33], v[28:29]
	buffer_load_dwordx4 v[26:29], v25, s[0:3], s10 offen offset:2048 nt
	v_pk_fma_f32 v[54:55], v[8:9], v[30:31], v[54:55]
	buffer_load_dwordx4 v[30:33], v25, s[0:3], s10 offen offset:3072 nt
	v_add_f32_e32 v66, v54, v55
	s_waitcnt vmcnt(7)
	v_pk_mul_f32 v[54:55], v[6:7], v[44:45]
	v_pk_mul_f32 v[56:57], v[4:5], v[42:43]
	buffer_load_dwordx4 v[42:45], v25, s[0:3], s5 offen offset:1024 nt
	s_waitcnt vmcnt(7)
	v_pk_fma_f32 v[54:55], v[2:3], v[36:37], v[54:55]
	v_pk_fma_f32 v[56:57], v[0:1], v[34:35], v[56:57]
	buffer_load_dwordx4 v[34:37], v25, s[0:3], s5 offen nt
	v_add_f32_dpp v18, v18, v18 quad_perm:[2,3,0,1] row_mask:0xf bank_mask:0xf bound_ctrl:1
	s_waitcnt vmcnt(7)
	v_pk_fma_f32 v[22:23], v[14:15], v[22:23], v[54:55]
	v_pk_fma_f32 v[20:21], v[12:13], v[20:21], v[56:57]
	s_waitcnt vmcnt(6)
	v_pk_fma_f32 v[60:61], v[10:11], v[48:49], v[22:23]
	v_pk_fma_f32 v[22:23], v[8:9], v[46:47], v[20:21]
	s_waitcnt vmcnt(4)
	v_pk_mul_f32 v[54:55], v[4:5], v[50:51]
	v_pk_mul_f32 v[20:21], v[6:7], v[52:53]
	v_pk_fma_f32 v[38:39], v[0:1], v[38:39], v[54:55]
	buffer_load_dwordx4 v[46:49], v25, s[0:3], s5 offen offset:2048 nt
	buffer_load_dwordx4 v[50:53], v25, s[0:3], s5 offen offset:3072 nt
	v_pk_fma_f32 v[20:21], v[2:3], v[40:41], v[20:21]
	v_add_f32_e32 v23, v22, v23
	v_add_f32_dpp v18, v18, v18 row_ror:4 row_mask:0xf bank_mask:0xf bound_ctrl:1
	s_waitcnt vmcnt(5)
	v_pk_fma_f32 v[26:27], v[12:13], v[26:27], v[38:39]
	buffer_load_dwordx4 v[38:41], v25, s[0:3], s4 offen nt
	buffer_load_dwordx4 v[54:57], v25, s[0:3], s4 offen offset:1024 nt
	v_pk_fma_f32 v[20:21], v[14:15], v[28:29], v[20:21]
	s_waitcnt vmcnt(6)
	v_pk_fma_f32 v[30:31], v[8:9], v[30:31], v[26:27]
	v_pk_fma_f32 v[62:63], v[10:11], v[32:33], v[20:21]
	v_add_f32_dpp v18, v18, v18 row_ror:8 row_mask:0xf bank_mask:0xf bound_ctrl:1
	s_waitcnt vmcnt(5)
	v_pk_mul_f32 v[20:21], v[6:7], v[44:45]
	v_pk_mul_f32 v[26:27], v[4:5], v[42:43]
	buffer_load_dwordx4 v[42:45], v25, s[0:3], s4 offen offset:2048 nt
	s_waitcnt vmcnt(5)
	v_pk_fma_f32 v[64:65], v[0:1], v[34:35], v[26:27]
	buffer_load_dwordx4 v[32:35], v25, s[0:3], s4 offen offset:3072 nt
	v_add_f32_e32 v27, v60, v61
	v_add_f32_e32 v23, v23, v27
	v_pk_fma_f32 v[36:37], v[2:3], v[36:37], v[20:21]
	v_add_f32_e32 v20, v58, v59
	v_add_f32_dpp v23, v23, v23 quad_perm:[1,0,3,2] row_mask:0xf bank_mask:0xf bound_ctrl:1
	v_add_f32_e32 v20, v66, v20
	v_mov_b32_e32 v19, v18
	v_add_f32_dpp v23, v23, v23 quad_perm:[2,3,0,1] row_mask:0xf bank_mask:0xf bound_ctrl:1
	v_add_f32_dpp v20, v20, v20 quad_perm:[1,0,3,2] row_mask:0xf bank_mask:0xf bound_ctrl:1
	v_permlane16_swap_b32_e32 v18, v19
	v_add_f32_dpp v23, v23, v23 row_ror:4 row_mask:0xf bank_mask:0xf bound_ctrl:1
	v_add_f32_dpp v20, v20, v20 quad_perm:[2,3,0,1] row_mask:0xf bank_mask:0xf bound_ctrl:1
	v_add_f32_e32 v18, v18, v19
	v_add_f32_dpp v23, v23, v23 row_ror:8 row_mask:0xf bank_mask:0xf bound_ctrl:1
	v_mov_b32_e32 v27, v23
	s_nop 1
	v_permlane16_swap_b32_e32 v23, v27
	v_add_f32_e32 v28, v23, v27
	v_add_f32_e32 v23, v30, v31
	s_waitcnt vmcnt(5)
	v_pk_fma_f32 v[30:31], v[14:15], v[48:49], v[36:37]
	v_pk_fma_f32 v[36:37], v[12:13], v[46:47], v[64:65]
	s_waitcnt vmcnt(4)
	v_pk_fma_f32 v[30:31], v[10:11], v[52:53], v[30:31]
	v_pk_fma_f32 v[36:37], v[8:9], v[50:51], v[36:37]
	v_add_f32_e32 v27, v62, v63
	v_add_f32_e32 v36, v36, v37
	v_add_f32_e32 v30, v30, v31
	v_add_f32_e32 v23, v23, v27
	v_add_f32_e32 v30, v36, v30
	v_add_f32_dpp v20, v20, v20 row_ror:4 row_mask:0xf bank_mask:0xf bound_ctrl:1
	v_add_f32_dpp v23, v23, v23 quad_perm:[1,0,3,2] row_mask:0xf bank_mask:0xf bound_ctrl:1
	v_add_f32_dpp v30, v30, v30 quad_perm:[1,0,3,2] row_mask:0xf bank_mask:0xf bound_ctrl:1
	v_add_f32_dpp v20, v20, v20 row_ror:8 row_mask:0xf bank_mask:0xf bound_ctrl:1
	v_add_f32_dpp v23, v23, v23 quad_perm:[2,3,0,1] row_mask:0xf bank_mask:0xf bound_ctrl:1
	v_add_f32_dpp v30, v30, v30 quad_perm:[2,3,0,1] row_mask:0xf bank_mask:0xf bound_ctrl:1
	v_mov_b32_e32 v21, v20
	v_add_f32_dpp v23, v23, v23 row_ror:4 row_mask:0xf bank_mask:0xf bound_ctrl:1
	v_add_f32_dpp v30, v30, v30 row_ror:4 row_mask:0xf bank_mask:0xf bound_ctrl:1
	v_permlane16_swap_b32_e32 v20, v21
	v_add_f32_dpp v23, v23, v23 row_ror:8 row_mask:0xf bank_mask:0xf bound_ctrl:1
	v_add_f32_dpp v30, v30, v30 row_ror:8 row_mask:0xf bank_mask:0xf bound_ctrl:1
	v_mov_b32_e32 v27, v23
	v_mov_b32_e32 v31, v30
	s_nop 0
	v_permlane16_swap_b32_e32 v23, v27
	v_permlane16_swap_b32_e32 v30, v31
	v_add_f32_e32 v21, v20, v21
	v_add_f32_e32 v23, v23, v27
	v_add_f32_e32 v30, v30, v31
	v_mov_b32_e32 v19, v16
	v_mov_b32_e32 v20, v17
	v_mov_b32_e32 v22, v18
	v_mov_b32_e32 v26, v21
	v_mov_b32_e32 v29, v28
	v_mov_b32_e32 v27, v23
	v_mov_b32_e32 v31, v30
	v_permlane32_swap_b32_e32 v16, v19
	v_permlane32_swap_b32_e32 v17, v20
	v_permlane32_swap_b32_e32 v18, v22
	v_permlane32_swap_b32_e32 v21, v26
	v_permlane32_swap_b32_e32 v28, v29
	v_permlane32_swap_b32_e32 v23, v27
	s_waitcnt vmcnt(2)
	v_pk_mul_f32 v[6:7], v[6:7], v[56:57]
	v_pk_mul_f32 v[4:5], v[4:5], v[54:55]
	v_pk_fma_f32 v[2:3], v[2:3], v[40:41], v[6:7]
	v_pk_fma_f32 v[0:1], v[0:1], v[38:39], v[4:5]
	v_permlane32_swap_b32_e32 v30, v31
	s_waitcnt vmcnt(1)
	v_pk_fma_f32 v[2:3], v[14:15], v[44:45], v[2:3]
	v_pk_fma_f32 v[0:1], v[12:13], v[42:43], v[0:1]
	s_waitcnt vmcnt(0)
	v_pk_fma_f32 v[2:3], v[10:11], v[34:35], v[2:3]
	v_pk_fma_f32 v[0:1], v[8:9], v[32:33], v[0:1]
	s_nop 0
	v_add_f32_e32 v0, v0, v1
	v_add_f32_e32 v1, v2, v3
	v_add_f32_e32 v0, v0, v1
	s_nop 1
	v_add_f32_dpp v0, v0, v0 quad_perm:[1,0,3,2] row_mask:0xf bank_mask:0xf bound_ctrl:1
	s_nop 1
	v_add_f32_dpp v0, v0, v0 quad_perm:[2,3,0,1] row_mask:0xf bank_mask:0xf bound_ctrl:1
	s_nop 1
	v_add_f32_dpp v0, v0, v0 row_ror:4 row_mask:0xf bank_mask:0xf bound_ctrl:1
	s_nop 1
	v_add_f32_dpp v0, v0, v0 row_ror:8 row_mask:0xf bank_mask:0xf bound_ctrl:1
	v_mov_b32_e32 v1, v0
	s_nop 1
	v_permlane16_swap_b32_e32 v0, v1
	v_add_f32_e32 v0, v0, v1
	v_mov_b32_e32 v1, v0
	s_nop 1
	v_permlane32_swap_b32_e32 v0, v1
	s_and_saveexec_b64 s[0:1], vcc
	s_cbranch_execz .LBB1_4
	v_add_f32_e32 v6, v16, v19
	v_cmp_eq_u32_e32 vcc, 0, v24
	v_add_f32_e32 v5, v17, v20
	v_add_f32_e32 v4, v18, v22
	v_cndmask_b32_e32 v6, 0, v6, vcc
	v_cmp_eq_u32_e32 vcc, 1, v24
	v_add_f32_e32 v3, v21, v26
	v_add_f32_e32 v2, v28, v29
	v_cndmask_b32_e32 v5, v6, v5, vcc
	v_cmp_eq_u32_e32 vcc, 2, v24
	v_add_f32_e32 v0, v0, v1
	v_add_f32_e32 v1, v30, v31
	v_cndmask_b32_e32 v4, v5, v4, vcc
	v_cmp_eq_u32_e32 vcc, 3, v24
	s_lshl_b32 s0, s8, 13
	s_and_b32 s0, s0, 0x1e000
	v_cndmask_b32_e32 v3, v4, v3, vcc
	v_cmp_eq_u32_e32 vcc, 4, v24
	s_add_u32 s0, s6, s0
	s_addc_u32 s1, s7, 0
	v_cndmask_b32_e32 v2, v3, v2, vcc
	v_add_f32_e32 v3, v23, v27
	v_cmp_eq_u32_e32 vcc, 5, v24
	s_nop 1
	v_cndmask_b32_e32 v2, v2, v3, vcc
	v_cmp_eq_u32_e32 vcc, 6, v24
	s_nop 1
	v_cndmask_b32_e32 v1, v2, v1, vcc
	v_cmp_eq_u32_e32 vcc, 7, v24
	s_nop 1
	v_cndmask_b32_e32 v2, v1, v0, vcc
	v_add_u32_e32 v0, s9, v25
	v_ashrrev_i32_e32 v0, 4, v0
	v_ashrrev_i32_e32 v1, 31, v0
	v_lshl_add_u64 v[0:1], v[0:1], 2, s[0:1]
	v_add_co_u32_e32 v0, vcc, 0x6000, v0
	s_nop 1
	v_addc_co_u32_e32 v1, vcc, 0, v1, vcc
	global_store_dword v[0:1], v2, off offset:64
